# baseline (speedup 1.0000x reference)
.LBB2_26:
	s_waitcnt lgkmcnt(0)
	ds_read_b64_tr_b16 v[156:157], v223 offset:0
	ds_read_b64_tr_b16 v[158:159], v223 offset:0x800
	ds_read_b64_tr_b16 v[152:153], v223 offset:0x200
	ds_read_b64_tr_b16 v[154:155], v223 offset:0xa00
	ds_read_b64_tr_b16 v[148:149], v223 offset:0x400
	ds_read_b64_tr_b16 v[150:151], v223 offset:0xc00
	ds_read_b64_tr_b16 v[144:145], v223 offset:0x600
	ds_read_b64_tr_b16 v[146:147], v223 offset:0xe00
	ds_read_b64_tr_b16 v[140:141], v223 offset:0x1000
	ds_read_b64_tr_b16 v[142:143], v223 offset:0x1800
	ds_read_b64_tr_b16 v[136:137], v223 offset:0x1200
	ds_read_b64_tr_b16 v[138:139], v223 offset:0x1a00
	ds_read_b64_tr_b16 v[132:133], v223 offset:0x1400
	ds_read_b64_tr_b16 v[134:135], v223 offset:0x1c00
	ds_read_b64_tr_b16 v[128:129], v223 offset:0x1600
	ds_read_b64_tr_b16 v[130:131], v223 offset:0x1e00
	ds_read_b64_tr_b16 v[124:125], v223 offset:0x2000
	ds_read_b64_tr_b16 v[126:127], v223 offset:0x2800
	v_exp_f32_e32 v48, v48
	v_exp_f32_e32 v49, v49
	ds_read_b64_tr_b16 v[120:121], v223 offset:0x2200
	ds_read_b64_tr_b16 v[122:123], v223 offset:0x2a00
	ds_read_b64_tr_b16 v[116:117], v223 offset:0x2400
	ds_read_b64_tr_b16 v[118:119], v223 offset:0x2c00
	v_exp_f32_e32 v190, v44
	v_cvt_pk_bf16_f32 v44, v48, v49
	v_add_f32_e32 v48, v161, v48
	v_add_f32_e32 v49, v160, v49
	ds_read_b64_tr_b16 v[112:113], v223 offset:0x2600
	v_exp_f32_e32 v164, v50
	v_exp_f32_e32 v165, v51
	v_add_f32_e32 v48, v48, v164
	v_add_f32_e32 v49, v49, v165
	ds_read_b64_tr_b16 v[114:115], v223 offset:0x2e00
	v_exp_f32_e32 v166, v52
	v_exp_f32_e32 v167, v53
	v_add_f32_e32 v48, v48, v166
	v_add_f32_e32 v49, v49, v167
	ds_read_b64_tr_b16 v[108:109], v223 offset:0x3000
	v_exp_f32_e32 v168, v54
	v_exp_f32_e32 v169, v55
	v_exp_f32_e32 v178, v32
	v_cvt_pk_bf16_f32 v51, v66, v67
	v_add_f32_e32 v48, v48, v168
	v_add_f32_e32 v49, v49, v169
	v_add_f32_e32 v66, v162, v178
	ds_read_b64_tr_b16 v[110:111], v223 offset:0x3800
	v_exp_f32_e32 v170, v56
	v_exp_f32_e32 v171, v57
	v_exp_f32_e32 v179, v33
	v_exp_f32_e32 v180, v34
	v_add_f32_e32 v48, v48, v170
	v_add_f32_e32 v49, v49, v171
	v_add_f32_e32 v67, v163, v179
	v_add_f32_e32 v66, v66, v180
	ds_read_b64_tr_b16 v[104:105], v223 offset:0x3200
	v_exp_f32_e32 v172, v58
	v_exp_f32_e32 v173, v59
	v_exp_f32_e32 v181, v35
	v_exp_f32_e32 v182, v36
	v_add_f32_e32 v48, v48, v172
	v_add_f32_e32 v49, v49, v173
	v_add_f32_e32 v67, v67, v181
	v_add_f32_e32 v66, v66, v182
	ds_read_b64_tr_b16 v[106:107], v223 offset:0x3a00
	v_exp_f32_e32 v174, v60
	v_exp_f32_e32 v175, v61
	v_exp_f32_e32 v183, v37
	v_exp_f32_e32 v184, v38
	v_add_f32_e32 v48, v48, v174
	v_add_f32_e32 v49, v49, v175
	v_add_f32_e32 v67, v67, v183
	v_add_f32_e32 v66, v66, v184
	ds_read_b64_tr_b16 v[100:101], v223 offset:0x3400
	v_exp_f32_e32 v176, v62
	v_exp_f32_e32 v177, v63
	v_exp_f32_e32 v185, v39
	v_exp_f32_e32 v186, v40
	v_add_f32_e32 v48, v48, v176
	v_add_f32_e32 v49, v49, v177
	v_add_f32_e32 v67, v67, v185
	v_add_f32_e32 v66, v66, v186
	ds_read_b64_tr_b16 v[102:103], v223 offset:0x3c00
	v_exp_f32_e32 v187, v41
	v_exp_f32_e32 v188, v42
	v_add_f32_e32 v67, v67, v187
	v_add_f32_e32 v66, v66, v188
	v_add_f32_e32 v48, v48, v49
	ds_read_b64_tr_b16 v[96:97], v223 offset:0x3600
	v_exp_f32_e32 v189, v43
	v_mov_b32_e32 v49, v48
	v_exp_f32_e32 v191, v45
	v_exp_f32_e32 v192, v46
	v_exp_f32_e32 v193, v47
	v_add_f32_e32 v67, v67, v189
	v_add_f32_e32 v66, v66, v190
	v_permlane32_swap_b32_e32 v48, v49
	ds_read_b64_tr_b16 v[98:99], v223 offset:0x3e00
	s_nop 1
	s_nop 1
	s_nop 1
	s_nop 1
	s_nop 1
	s_nop 1
	s_nop 1
	s_nop 1
	s_nop 1
	s_nop 1
	s_nop 1
	s_nop 1
	s_nop 1
	s_nop 1
	v_add_f32_e32 v67, v67, v191
	s_nop 1
	v_add_f32_e32 v66, v66, v192
	s_nop 1
	v_add_f32_e32 v48, v48, v49
	s_waitcnt lgkmcnt(0)
	s_nop 0
	v_cvt_pk_bf16_f32 v50, v64, v65
	v_add_f32_e32 v67, v67, v193
	v_add_f32_e32 v49, v231, v48
	v_cvt_pk_bf16_f32 v52, v68, v69
	v_add_f32_e32 v48, v66, v67
	v_cvt_pk_bf16_f32 v36, v72, v73
	v_mov_b32_e32 v66, v48
	s_nop 1
	v_permlane32_swap_b32_e32 v48, v66
	v_cvt_pk_bf16_f32 v37, v74, v75
	v_cvt_pk_bf16_f32 v38, v76, v77
	v_cvt_pk_bf16_f32 v39, v78, v79
	v_cvt_pk_bf16_f32 v45, v164, v165
	v_cvt_pk_bf16_f32 v46, v166, v167
	v_cvt_pk_bf16_f32 v47, v168, v169
	v_cvt_pk_bf16_f32 v32, v170, v171
	v_cvt_pk_bf16_f32 v33, v172, v173
	v_cvt_pk_bf16_f32 v34, v174, v175
	v_cvt_pk_bf16_f32 v35, v176, v177
	v_cvt_pk_bf16_f32 v40, v186, v187
	v_cvt_pk_bf16_f32 v41, v188, v189
	v_cvt_pk_bf16_f32 v42, v190, v191
	v_cvt_pk_bf16_f32 v43, v192, v193
	v_add_f32_e32 v48, v48, v66
	v_cvt_pk_bf16_f32 v53, v70, v71
	v_cvt_pk_bf16_f32 v54, v80, v81
	v_cvt_pk_bf16_f32 v55, v82, v83
	v_cvt_pk_bf16_f32 v56, v84, v85
	v_cvt_pk_bf16_f32 v57, v86, v87
	v_cvt_pk_bf16_f32 v58, v88, v89
	v_cvt_pk_bf16_f32 v59, v90, v91
	v_cvt_pk_bf16_f32 v60, v92, v93
	v_cvt_pk_bf16_f32 v61, v94, v95
	v_cvt_pk_bf16_f32 v62, v178, v179
	v_cvt_pk_bf16_f32 v63, v180, v181
	v_cvt_pk_bf16_f32 v64, v182, v183
	v_cvt_pk_bf16_f32 v65, v184, v185
	v_add_f32_e32 v48, v230, v48
	s_nop 1
	v_mfma_f32_32x32x16_bf16 a[0:15], v[156:159], v[50:53], a[0:15]
	s_nop 0
	v_mfma_f32_32x32x16_bf16 a[16:31], v[156:159], v[54:57], a[16:31]
	s_nop 0
	v_mfma_f32_32x32x16_bf16 a[32:47], v[152:155], v[50:53], a[32:47]
	s_nop 0
	v_mfma_f32_32x32x16_bf16 a[48:63], v[152:155], v[54:57], a[48:63]
	s_nop 0
	v_mfma_f32_32x32x16_bf16 a[64:79], v[148:151], v[50:53], a[64:79]
	s_nop 0
	v_mfma_f32_32x32x16_bf16 a[80:95], v[148:151], v[54:57], a[80:95]
	s_nop 0
	v_mfma_f32_32x32x16_bf16 a[96:111], v[144:147], v[50:53], a[96:111]
	s_nop 0
	v_mfma_f32_32x32x16_bf16 a[112:127], v[144:147], v[54:57], a[112:127]
	s_nop 0
	v_mfma_f32_32x32x16_bf16 a[0:15], v[140:143], v[36:39], a[0:15]
	s_nop 0
	v_mfma_f32_32x32x16_bf16 a[16:31], v[140:143], v[58:61], a[16:31]
	s_nop 0
	v_mfma_f32_32x32x16_bf16 a[32:47], v[136:139], v[36:39], a[32:47]
	s_nop 0
	v_mfma_f32_32x32x16_bf16 a[48:63], v[136:139], v[58:61], a[48:63]
	s_nop 0
	v_mfma_f32_32x32x16_bf16 a[64:79], v[132:135], v[36:39], a[64:79]
	s_nop 0
	v_mfma_f32_32x32x16_bf16 a[80:95], v[132:135], v[58:61], a[80:95]
	s_nop 0
	v_mfma_f32_32x32x16_bf16 a[96:111], v[128:131], v[36:39], a[96:111]
	s_nop 0
	v_mfma_f32_32x32x16_bf16 a[112:127], v[128:131], v[58:61], a[112:127]
	s_nop 0
	v_mfma_f32_32x32x16_bf16 a[0:15], v[124:127], v[44:47], a[0:15]
	s_nop 0
	v_mfma_f32_32x32x16_bf16 a[16:31], v[124:127], v[62:65], a[16:31]
	s_nop 0
	v_mfma_f32_32x32x16_bf16 a[32:47], v[120:123], v[44:47], a[32:47]
	s_nop 0
	v_mfma_f32_32x32x16_bf16 a[48:63], v[120:123], v[62:65], a[48:63]
	s_nop 0
	v_mfma_f32_32x32x16_bf16 a[64:79], v[116:119], v[44:47], a[64:79]
	s_nop 0
	v_mfma_f32_32x32x16_bf16 a[80:95], v[116:119], v[62:65], a[80:95]
	s_nop 0
	v_mfma_f32_32x32x16_bf16 a[96:111], v[112:115], v[44:47], a[96:111]
	s_nop 0
	v_mfma_f32_32x32x16_bf16 a[112:127], v[112:115], v[62:65], a[112:127]
	s_nop 0
	v_mfma_f32_32x32x16_bf16 a[0:15], v[108:111], v[32:35], a[0:15]
	s_nop 0
	v_mfma_f32_32x32x16_bf16 a[16:31], v[108:111], v[40:43], a[16:31]
	s_nop 0
	v_mfma_f32_32x32x16_bf16 a[32:47], v[104:107], v[32:35], a[32:47]
	s_nop 0
	v_mfma_f32_32x32x16_bf16 a[48:63], v[104:107], v[40:43], a[48:63]
	s_nop 0
	v_mfma_f32_32x32x16_bf16 a[64:79], v[100:103], v[32:35], a[64:79]
	s_nop 0
	v_mfma_f32_32x32x16_bf16 a[80:95], v[100:103], v[40:43], a[80:95]
	s_nop 0
	v_mfma_f32_32x32x16_bf16 a[96:111], v[96:99], v[32:35], a[96:111]
	s_nop 0
	v_mfma_f32_32x32x16_bf16 a[112:127], v[96:99], v[40:43], a[112:127]
	v_rcp_f32_e32 v34, v49
	s_nop 7
	s_nop 7
	v_mov_b32_e32 v132, v48
	v_cmp_lt_f32_e32 vcc, 0, v49
	v_cndmask_b32_e32 v43, 0, v34, vcc
	v_lshrrev_b32_e32 v42, 4, v225
	s_lshl_b32 s4, s26, 11
	v_mov_b32_e32 v33, s29
	v_or_b32_e32 v32, s28, v200
	s_and_b32 s24, s4, 0x3800
	v_lshl_add_u64 v[34:35], s[24:25], 0, v[32:33]
	v_lshlrev_b32_e32 v39, 8, v42
	v_lshlrev_b32_e32 v32, 4, v225
	v_and_or_b32 v200, v32, s80, v39
	v_lshl_add_u64 v[32:33], s[14:15], 0, v[200:201]
	v_lshlrev_b64 v[34:35], 8, v[34:35]
	v_lshl_add_u64 v[124:125], v[32:33], 0, v[34:35]
	v_mov_b32_e32 v34, 0x1000
	v_mov_b32_e32 v35, 0
	v_lshl_add_u64 v[126:127], v[124:125], 0, v[34:35]
	v_lshl_add_u64 v[128:129], v[126:127], 0, v[34:35]
	v_lshl_add_u64 v[130:131], v[128:129], 0, v[34:35]
	v_and_b32_e32 v32, 31, v225
	v_lshl_add_u32 v36, v32, 8, v214
	v_and_b32_e32 v37, 15, v225
	v_lshlrev_b32_e32 v37, 4, v37
	v_lshrrev_b32_e32 v38, 5, v225
	v_lshlrev_b32_e32 v38, 3, v38
	v_xad_u32 v100, v38, v37, v36
	v_add_u32_e32 v101, 0x10, v38
	v_xad_u32 v101, v101, v37, v36
	v_add_u32_e32 v102, 0x20, v38
	v_xad_u32 v102, v102, v37, v36
	v_add_u32_e32 v103, 0x30, v38
	v_xad_u32 v103, v103, v37, v36
	v_add_u32_e32 v104, 0x40, v38
	v_xad_u32 v104, v104, v37, v36
	v_add_u32_e32 v105, 0x50, v38
	v_xad_u32 v105, v105, v37, v36
	v_add_u32_e32 v106, 0x60, v38
	v_xad_u32 v106, v106, v37, v36
	v_add_u32_e32 v107, 0x70, v38
	v_xad_u32 v107, v107, v37, v36
	v_add_u32_e32 v108, 0x80, v38
	v_xad_u32 v108, v108, v37, v36
	v_add_u32_e32 v109, 0x90, v38
	v_xad_u32 v109, v109, v37, v36
	v_add_u32_e32 v110, 0xa0, v38
	v_xad_u32 v110, v110, v37, v36
	v_add_u32_e32 v111, 0xb0, v38
	v_xad_u32 v111, v111, v37, v36
	v_add_u32_e32 v112, 0xc0, v38
	v_xad_u32 v112, v112, v37, v36
	v_add_u32_e32 v113, 0xd0, v38
	v_xad_u32 v113, v113, v37, v36
	v_add_u32_e32 v114, 0xe0, v38
	v_xad_u32 v114, v114, v37, v36
	v_add_u32_e32 v115, 0xf0, v38
	v_xad_u32 v115, v115, v37, v36
	v_and_b32_e32 v33, 15, v225
	v_mov_b32_e32 v116, v42
	v_and_b32_e32 v39, 15, v116
	v_xor_b32_e32 v39, v39, v33
	v_lshlrev_b32_e32 v39, 4, v39
	v_lshl_add_u32 v116, v116, 8, v214
	v_add_u32_e32 v116, v116, v39
	v_add_u32_e32 v117, 4, v42
	v_and_b32_e32 v39, 15, v117
	v_xor_b32_e32 v39, v39, v33
	v_lshlrev_b32_e32 v39, 4, v39
	v_lshl_add_u32 v117, v117, 8, v214
	v_add_u32_e32 v117, v117, v39
	v_add_u32_e32 v118, 8, v42
	v_and_b32_e32 v39, 15, v118
	v_xor_b32_e32 v39, v39, v33
	v_lshlrev_b32_e32 v39, 4, v39
	v_lshl_add_u32 v118, v118, 8, v214
	v_add_u32_e32 v118, v118, v39
	v_add_u32_e32 v119, 12, v42
	v_and_b32_e32 v39, 15, v119
	v_xor_b32_e32 v39, v39, v33
	v_lshlrev_b32_e32 v39, 4, v39
	v_lshl_add_u32 v119, v119, 8, v214
	v_add_u32_e32 v119, v119, v39
	v_add_u32_e32 v120, 16, v42
	v_and_b32_e32 v39, 15, v120
	v_xor_b32_e32 v39, v39, v33
	v_lshlrev_b32_e32 v39, 4, v39
	v_lshl_add_u32 v120, v120, 8, v214
	v_add_u32_e32 v120, v120, v39
	v_add_u32_e32 v121, 20, v42
	v_and_b32_e32 v39, 15, v121
	v_xor_b32_e32 v39, v39, v33
	v_lshlrev_b32_e32 v39, 4, v39
	v_lshl_add_u32 v121, v121, 8, v214
	v_add_u32_e32 v121, v121, v39
	v_add_u32_e32 v122, 24, v42
	v_and_b32_e32 v39, 15, v122
	v_xor_b32_e32 v39, v39, v33
	v_lshlrev_b32_e32 v39, 4, v39
	v_lshl_add_u32 v122, v122, 8, v214
	v_add_u32_e32 v122, v122, v39
	v_add_u32_e32 v123, 28, v42
	v_and_b32_e32 v39, 15, v123
	v_xor_b32_e32 v39, v39, v33
	v_lshlrev_b32_e32 v39, 4, v39
	v_lshl_add_u32 v123, v123, 8, v214
	v_add_u32_e32 v123, v123, v39
	v_accvgpr_read_b32 v64, a0
	v_accvgpr_read_b32 v65, a1
	v_accvgpr_read_b32 v66, a2
	v_accvgpr_read_b32 v67, a3
	v_accvgpr_read_b32 v68, a4
	v_accvgpr_read_b32 v69, a5
	v_accvgpr_read_b32 v70, a6
	v_accvgpr_read_b32 v71, a7
	v_accvgpr_read_b32 v72, a8
	v_accvgpr_read_b32 v73, a9
	v_accvgpr_read_b32 v74, a10
	v_accvgpr_read_b32 v75, a11
	v_accvgpr_read_b32 v76, a12
	v_accvgpr_read_b32 v77, a13
	v_accvgpr_read_b32 v78, a14
	v_accvgpr_read_b32 v79, a15
	v_mul_f32_e32 v64, v64, v43
	v_mul_f32_e32 v65, v65, v43
	v_mul_f32_e32 v66, v66, v43
	v_mul_f32_e32 v67, v67, v43
	v_mul_f32_e32 v68, v68, v43
	v_mul_f32_e32 v69, v69, v43
	v_mul_f32_e32 v70, v70, v43
	v_mul_f32_e32 v71, v71, v43
	v_mul_f32_e32 v72, v72, v43
	v_mul_f32_e32 v73, v73, v43
	v_mul_f32_e32 v74, v74, v43
	v_mul_f32_e32 v75, v75, v43
	v_mul_f32_e32 v76, v76, v43
	v_mul_f32_e32 v77, v77, v43
	v_mul_f32_e32 v78, v78, v43
	v_mul_f32_e32 v79, v79, v43
	v_cvt_pk_f16_f32 v80, v64, v65
	v_cvt_pk_f16_f32 v81, v66, v67
	v_cvt_pk_f16_f32 v82, v68, v69
	v_cvt_pk_f16_f32 v83, v70, v71
	v_cvt_pk_f16_f32 v84, v72, v73
	v_cvt_pk_f16_f32 v85, v74, v75
	v_cvt_pk_f16_f32 v86, v76, v77
	v_cvt_pk_f16_f32 v87, v78, v79
	ds_write_b64 v100, v[80:81]
	ds_write_b64 v101, v[82:83]
	ds_write_b64 v102, v[84:85]
	ds_write_b64 v103, v[86:87]
	v_accvgpr_read_b32 v64, a32
	v_accvgpr_read_b32 v65, a33
	v_accvgpr_read_b32 v66, a34
	v_accvgpr_read_b32 v67, a35
	v_accvgpr_read_b32 v68, a36
	v_accvgpr_read_b32 v69, a37
	v_accvgpr_read_b32 v70, a38
	v_accvgpr_read_b32 v71, a39
	v_accvgpr_read_b32 v72, a40
	v_accvgpr_read_b32 v73, a41
	v_accvgpr_read_b32 v74, a42
	v_accvgpr_read_b32 v75, a43
	v_accvgpr_read_b32 v76, a44
	v_accvgpr_read_b32 v77, a45
	v_accvgpr_read_b32 v78, a46
	v_accvgpr_read_b32 v79, a47
	v_mul_f32_e32 v64, v64, v43
	v_mul_f32_e32 v65, v65, v43
	v_mul_f32_e32 v66, v66, v43
	v_mul_f32_e32 v67, v67, v43
	v_mul_f32_e32 v68, v68, v43
	v_mul_f32_e32 v69, v69, v43
	v_mul_f32_e32 v70, v70, v43
	v_mul_f32_e32 v71, v71, v43
	v_mul_f32_e32 v72, v72, v43
	v_mul_f32_e32 v73, v73, v43
	v_mul_f32_e32 v74, v74, v43
	v_mul_f32_e32 v75, v75, v43
	v_mul_f32_e32 v76, v76, v43
	v_mul_f32_e32 v77, v77, v43
	v_mul_f32_e32 v78, v78, v43
	v_mul_f32_e32 v79, v79, v43
	v_cvt_pk_f16_f32 v80, v64, v65
	v_cvt_pk_f16_f32 v81, v66, v67
	v_cvt_pk_f16_f32 v82, v68, v69
	v_cvt_pk_f16_f32 v83, v70, v71
	v_cvt_pk_f16_f32 v84, v72, v73
	v_cvt_pk_f16_f32 v85, v74, v75
	v_cvt_pk_f16_f32 v86, v76, v77
	v_cvt_pk_f16_f32 v87, v78, v79
	ds_write_b64 v104, v[80:81]
	ds_write_b64 v105, v[82:83]
	ds_write_b64 v106, v[84:85]
	ds_write_b64 v107, v[86:87]
	v_accvgpr_read_b32 v64, a64
	v_accvgpr_read_b32 v65, a65
	v_accvgpr_read_b32 v66, a66
	v_accvgpr_read_b32 v67, a67
	v_accvgpr_read_b32 v68, a68
	v_accvgpr_read_b32 v69, a69
	v_accvgpr_read_b32 v70, a70
	v_accvgpr_read_b32 v71, a71
	v_accvgpr_read_b32 v72, a72
	v_accvgpr_read_b32 v73, a73
	v_accvgpr_read_b32 v74, a74
	v_accvgpr_read_b32 v75, a75
	v_accvgpr_read_b32 v76, a76
	v_accvgpr_read_b32 v77, a77
	v_accvgpr_read_b32 v78, a78
	v_accvgpr_read_b32 v79, a79
	v_mul_f32_e32 v64, v64, v43
	v_mul_f32_e32 v65, v65, v43
	v_mul_f32_e32 v66, v66, v43
	v_mul_f32_e32 v67, v67, v43
	v_mul_f32_e32 v68, v68, v43
	v_mul_f32_e32 v69, v69, v43
	v_mul_f32_e32 v70, v70, v43
	v_mul_f32_e32 v71, v71, v43
	v_mul_f32_e32 v72, v72, v43
	v_mul_f32_e32 v73, v73, v43
	v_mul_f32_e32 v74, v74, v43
	v_mul_f32_e32 v75, v75, v43
	v_mul_f32_e32 v76, v76, v43
	v_mul_f32_e32 v77, v77, v43
	v_mul_f32_e32 v78, v78, v43
	v_mul_f32_e32 v79, v79, v43
	v_cvt_pk_f16_f32 v80, v64, v65
	v_cvt_pk_f16_f32 v81, v66, v67
	v_cvt_pk_f16_f32 v82, v68, v69
	v_cvt_pk_f16_f32 v83, v70, v71
	v_cvt_pk_f16_f32 v84, v72, v73
	v_cvt_pk_f16_f32 v85, v74, v75
	v_cvt_pk_f16_f32 v86, v76, v77
	v_cvt_pk_f16_f32 v87, v78, v79
	ds_write_b64 v108, v[80:81]
	ds_write_b64 v109, v[82:83]
	ds_write_b64 v110, v[84:85]
	ds_write_b64 v111, v[86:87]
	v_accvgpr_read_b32 v64, a96
	v_accvgpr_read_b32 v65, a97
	v_accvgpr_read_b32 v66, a98
	v_accvgpr_read_b32 v67, a99
	v_accvgpr_read_b32 v68, a100
	v_accvgpr_read_b32 v69, a101
	v_accvgpr_read_b32 v70, a102
	v_accvgpr_read_b32 v71, a103
	v_accvgpr_read_b32 v72, a104
	v_accvgpr_read_b32 v73, a105
	v_accvgpr_read_b32 v74, a106
	v_accvgpr_read_b32 v75, a107
	v_accvgpr_read_b32 v76, a108
	v_accvgpr_read_b32 v77, a109
	v_accvgpr_read_b32 v78, a110
	v_accvgpr_read_b32 v79, a111
	v_mul_f32_e32 v64, v64, v43
	v_mul_f32_e32 v65, v65, v43
	v_mul_f32_e32 v66, v66, v43
	v_mul_f32_e32 v67, v67, v43
	v_mul_f32_e32 v68, v68, v43
	v_mul_f32_e32 v69, v69, v43
	v_mul_f32_e32 v70, v70, v43
	v_mul_f32_e32 v71, v71, v43
	v_mul_f32_e32 v72, v72, v43
	v_mul_f32_e32 v73, v73, v43
	v_mul_f32_e32 v74, v74, v43
	v_mul_f32_e32 v75, v75, v43
	v_mul_f32_e32 v76, v76, v43
	v_mul_f32_e32 v77, v77, v43
	v_mul_f32_e32 v78, v78, v43
	v_mul_f32_e32 v79, v79, v43
	v_cvt_pk_f16_f32 v80, v64, v65
	v_cvt_pk_f16_f32 v81, v66, v67
	v_cvt_pk_f16_f32 v82, v68, v69
	v_cvt_pk_f16_f32 v83, v70, v71
	v_cvt_pk_f16_f32 v84, v72, v73
	v_cvt_pk_f16_f32 v85, v74, v75
	v_cvt_pk_f16_f32 v86, v76, v77
	v_cvt_pk_f16_f32 v87, v78, v79
	ds_write_b64 v112, v[80:81]
	ds_write_b64 v113, v[82:83]
	ds_write_b64 v114, v[84:85]
	ds_write_b64 v115, v[86:87]
	s_waitcnt lgkmcnt(0)
	ds_read_b128 v[136:139], v116
	ds_read_b128 v[140:143], v117
	ds_read_b128 v[144:147], v118
	ds_read_b128 v[148:151], v119
	ds_read_b128 v[152:155], v120
	ds_read_b128 v[156:159], v121
	ds_read_b128 v[160:163], v122
	ds_read_b128 v[164:167], v123
	s_waitcnt lgkmcnt(7)
	global_store_dwordx4 v[124:125], v[136:139], off
	s_waitcnt lgkmcnt(6)
	global_store_dwordx4 v[124:125], v[140:143], off offset:1024
	s_waitcnt lgkmcnt(5)
	global_store_dwordx4 v[124:125], v[144:147], off offset:2048
	s_waitcnt lgkmcnt(4)
	global_store_dwordx4 v[124:125], v[148:151], off offset:3072
	s_waitcnt lgkmcnt(3)
	global_store_dwordx4 v[126:127], v[152:155], off
	s_waitcnt lgkmcnt(2)
	global_store_dwordx4 v[126:127], v[156:159], off offset:1024
	s_waitcnt lgkmcnt(1)
	global_store_dwordx4 v[126:127], v[160:163], off offset:2048
	s_waitcnt lgkmcnt(0)
	global_store_dwordx4 v[126:127], v[164:167], off offset:3072
	v_rcp_f32_e32 v34, v132
	s_nop 1
	v_cmp_lt_f32_e32 vcc, 0, v132
	v_cndmask_b32_e32 v43, 0, v34, vcc
	s_waitcnt lgkmcnt(0)
	v_accvgpr_read_b32 v64, a16
	v_accvgpr_read_b32 v65, a17
	v_accvgpr_read_b32 v66, a18
	v_accvgpr_read_b32 v67, a19
	v_accvgpr_read_b32 v68, a20
	v_accvgpr_read_b32 v69, a21
	v_accvgpr_read_b32 v70, a22
	v_accvgpr_read_b32 v71, a23
	v_accvgpr_read_b32 v72, a24
	v_accvgpr_read_b32 v73, a25
	v_accvgpr_read_b32 v74, a26
	v_accvgpr_read_b32 v75, a27
	v_accvgpr_read_b32 v76, a28
	v_accvgpr_read_b32 v77, a29
	v_accvgpr_read_b32 v78, a30
	v_accvgpr_read_b32 v79, a31
	v_mul_f32_e32 v64, v64, v43
	v_mul_f32_e32 v65, v65, v43
	v_mul_f32_e32 v66, v66, v43
	v_mul_f32_e32 v67, v67, v43
	v_mul_f32_e32 v68, v68, v43
	v_mul_f32_e32 v69, v69, v43
	v_mul_f32_e32 v70, v70, v43
	v_mul_f32_e32 v71, v71, v43
	v_mul_f32_e32 v72, v72, v43
	v_mul_f32_e32 v73, v73, v43
	v_mul_f32_e32 v74, v74, v43
	v_mul_f32_e32 v75, v75, v43
	v_mul_f32_e32 v76, v76, v43
	v_mul_f32_e32 v77, v77, v43
	v_mul_f32_e32 v78, v78, v43
	v_mul_f32_e32 v79, v79, v43
	v_cvt_pk_f16_f32 v80, v64, v65
	v_cvt_pk_f16_f32 v81, v66, v67
	v_cvt_pk_f16_f32 v82, v68, v69
	v_cvt_pk_f16_f32 v83, v70, v71
	v_cvt_pk_f16_f32 v84, v72, v73
	v_cvt_pk_f16_f32 v85, v74, v75
	v_cvt_pk_f16_f32 v86, v76, v77
	v_cvt_pk_f16_f32 v87, v78, v79
	ds_write_b64 v100, v[80:81]
	ds_write_b64 v101, v[82:83]
	ds_write_b64 v102, v[84:85]
	ds_write_b64 v103, v[86:87]
	v_accvgpr_read_b32 v64, a48
	v_accvgpr_read_b32 v65, a49
	v_accvgpr_read_b32 v66, a50
	v_accvgpr_read_b32 v67, a51
	v_accvgpr_read_b32 v68, a52
	v_accvgpr_read_b32 v69, a53
	v_accvgpr_read_b32 v70, a54
	v_accvgpr_read_b32 v71, a55
	v_accvgpr_read_b32 v72, a56
	v_accvgpr_read_b32 v73, a57
	v_accvgpr_read_b32 v74, a58
	v_accvgpr_read_b32 v75, a59
	v_accvgpr_read_b32 v76, a60
	v_accvgpr_read_b32 v77, a61
	v_accvgpr_read_b32 v78, a62
	v_accvgpr_read_b32 v79, a63
	v_mul_f32_e32 v64, v64, v43
	v_mul_f32_e32 v65, v65, v43
	v_mul_f32_e32 v66, v66, v43
	v_mul_f32_e32 v67, v67, v43
	v_mul_f32_e32 v68, v68, v43
	v_mul_f32_e32 v69, v69, v43
	v_mul_f32_e32 v70, v70, v43
	v_mul_f32_e32 v71, v71, v43
	v_mul_f32_e32 v72, v72, v43
	v_mul_f32_e32 v73, v73, v43
	v_mul_f32_e32 v74, v74, v43
	v_mul_f32_e32 v75, v75, v43
	v_mul_f32_e32 v76, v76, v43
	v_mul_f32_e32 v77, v77, v43
	v_mul_f32_e32 v78, v78, v43
	v_mul_f32_e32 v79, v79, v43
	v_cvt_pk_f16_f32 v80, v64, v65
	v_cvt_pk_f16_f32 v81, v66, v67
	v_cvt_pk_f16_f32 v82, v68, v69
	v_cvt_pk_f16_f32 v83, v70, v71
	v_cvt_pk_f16_f32 v84, v72, v73
	v_cvt_pk_f16_f32 v85, v74, v75
	v_cvt_pk_f16_f32 v86, v76, v77
	v_cvt_pk_f16_f32 v87, v78, v79
	ds_write_b64 v104, v[80:81]
	ds_write_b64 v105, v[82:83]
	ds_write_b64 v106, v[84:85]
	ds_write_b64 v107, v[86:87]
	v_accvgpr_read_b32 v64, a80
	v_accvgpr_read_b32 v65, a81
	v_accvgpr_read_b32 v66, a82
	v_accvgpr_read_b32 v67, a83
	v_accvgpr_read_b32 v68, a84
	v_accvgpr_read_b32 v69, a85
	v_accvgpr_read_b32 v70, a86
	v_accvgpr_read_b32 v71, a87
	v_accvgpr_read_b32 v72, a88
	v_accvgpr_read_b32 v73, a89
	v_accvgpr_read_b32 v74, a90
	v_accvgpr_read_b32 v75, a91
	v_accvgpr_read_b32 v76, a92
	v_accvgpr_read_b32 v77, a93
	v_accvgpr_read_b32 v78, a94
	v_accvgpr_read_b32 v79, a95
	v_mul_f32_e32 v64, v64, v43
	v_mul_f32_e32 v65, v65, v43
	v_mul_f32_e32 v66, v66, v43
	v_mul_f32_e32 v67, v67, v43
	v_mul_f32_e32 v68, v68, v43
	v_mul_f32_e32 v69, v69, v43
	v_mul_f32_e32 v70, v70, v43
	v_mul_f32_e32 v71, v71, v43
	v_mul_f32_e32 v72, v72, v43
	v_mul_f32_e32 v73, v73, v43
	v_mul_f32_e32 v74, v74, v43
	v_mul_f32_e32 v75, v75, v43
	v_mul_f32_e32 v76, v76, v43
	v_mul_f32_e32 v77, v77, v43
	v_mul_f32_e32 v78, v78, v43
	v_mul_f32_e32 v79, v79, v43
	v_cvt_pk_f16_f32 v80, v64, v65
	v_cvt_pk_f16_f32 v81, v66, v67
	v_cvt_pk_f16_f32 v82, v68, v69
	v_cvt_pk_f16_f32 v83, v70, v71
	v_cvt_pk_f16_f32 v84, v72, v73
	v_cvt_pk_f16_f32 v85, v74, v75
	v_cvt_pk_f16_f32 v86, v76, v77
	v_cvt_pk_f16_f32 v87, v78, v79
	ds_write_b64 v108, v[80:81]
	ds_write_b64 v109, v[82:83]
	ds_write_b64 v110, v[84:85]
	ds_write_b64 v111, v[86:87]
	v_accvgpr_read_b32 v64, a112
	v_accvgpr_read_b32 v65, a113
	v_accvgpr_read_b32 v66, a114
	v_accvgpr_read_b32 v67, a115
	v_accvgpr_read_b32 v68, a116
	v_accvgpr_read_b32 v69, a117
	v_accvgpr_read_b32 v70, a118
	v_accvgpr_read_b32 v71, a119
	v_accvgpr_read_b32 v72, a120
	v_accvgpr_read_b32 v73, a121
	v_accvgpr_read_b32 v74, a122
	v_accvgpr_read_b32 v75, a123
	v_accvgpr_read_b32 v76, a124
	v_accvgpr_read_b32 v77, a125
	v_accvgpr_read_b32 v78, a126
	v_accvgpr_read_b32 v79, a127
	v_mul_f32_e32 v64, v64, v43
	v_mul_f32_e32 v65, v65, v43
	v_mul_f32_e32 v66, v66, v43
	v_mul_f32_e32 v67, v67, v43
	v_mul_f32_e32 v68, v68, v43
	v_mul_f32_e32 v69, v69, v43
	v_mul_f32_e32 v70, v70, v43
	v_mul_f32_e32 v71, v71, v43
	v_mul_f32_e32 v72, v72, v43
	v_mul_f32_e32 v73, v73, v43
	v_mul_f32_e32 v74, v74, v43
	v_mul_f32_e32 v75, v75, v43
	v_mul_f32_e32 v76, v76, v43
	v_mul_f32_e32 v77, v77, v43
	v_mul_f32_e32 v78, v78, v43
	v_mul_f32_e32 v79, v79, v43
	v_cvt_pk_f16_f32 v80, v64, v65
	v_cvt_pk_f16_f32 v81, v66, v67
	v_cvt_pk_f16_f32 v82, v68, v69
	v_cvt_pk_f16_f32 v83, v70, v71
	v_cvt_pk_f16_f32 v84, v72, v73
	v_cvt_pk_f16_f32 v85, v74, v75
	v_cvt_pk_f16_f32 v86, v76, v77
	v_cvt_pk_f16_f32 v87, v78, v79
	ds_write_b64 v112, v[80:81]
	ds_write_b64 v113, v[82:83]
	ds_write_b64 v114, v[84:85]
	ds_write_b64 v115, v[86:87]
	s_waitcnt lgkmcnt(0)
	ds_read_b128 v[136:139], v116
	ds_read_b128 v[140:143], v117
	ds_read_b128 v[144:147], v118
	ds_read_b128 v[148:151], v119
	ds_read_b128 v[152:155], v120
	ds_read_b128 v[156:159], v121
	ds_read_b128 v[160:163], v122
	ds_read_b128 v[164:167], v123
	s_waitcnt lgkmcnt(7)
	global_store_dwordx4 v[128:129], v[136:139], off
	s_waitcnt lgkmcnt(6)
	global_store_dwordx4 v[128:129], v[140:143], off offset:1024
	s_waitcnt lgkmcnt(5)
	global_store_dwordx4 v[128:129], v[144:147], off offset:2048
	s_waitcnt lgkmcnt(4)
	global_store_dwordx4 v[128:129], v[148:151], off offset:3072
	s_waitcnt lgkmcnt(3)
	global_store_dwordx4 v[130:131], v[152:155], off
	s_waitcnt lgkmcnt(2)
	global_store_dwordx4 v[130:131], v[156:159], off offset:1024
	s_waitcnt lgkmcnt(1)
	global_store_dwordx4 v[130:131], v[160:163], off offset:2048
	s_waitcnt lgkmcnt(0)
	global_store_dwordx4 v[130:131], v[164:167], off offset:3072
	s_waitcnt lgkmcnt(0)
	s_add_u32 s26, s26, s34
	s_addc_u32 s27, s27, 0
	v_cmp_gt_u64_e32 vcc, s[26:27], v[202:203]
	s_cbranch_vccnz .LBB2_64
	s_branch .LBB2_3
